# k_out and k_csr: pointer kernarg loads hoisted to kernel entry (no scalar-load round trip in the dependent chain)
# speedup vs baseline: 1.0038x; 1.0012x over previous
_Z5k_csrPKiPKjP15HIP_vector_typeIiLj2EEPfPtS6_:
	s_load_dwordx2 s[4:5], s[0:1], 0x0
	s_load_dwordx2 s[84:85], s[0:1], 0x8
	v_lshlrev_b32_e32 v40, 2, v0
	v_mov_b32_e32 v1, 0
	v_cmp_eq_u32_e32 vcc, 0, v0
	ds_write_b32 v40, v1 offset:16384
	s_and_saveexec_b64 s[6:7], vcc
	ds_write_b32 v1, v1 offset:18448
	s_or_b64 exec, exec, s[6:7]
	v_lshl_or_b32 v36, s2, 8, v0
	v_ashrrev_i32_e32 v37, 31, v36
	s_waitcnt lgkmcnt(0)
	v_lshl_add_u64 v[2:3], v[36:37], 2, s[4:5]
	s_barrier
	global_load_dword v34, v[2:3], off
	v_add_u32_e32 v2, 0x100, v36
	v_ashrrev_i32_e32 v3, 31, v2
	v_lshl_add_u64 v[2:3], v[2:3], 2, s[4:5]
	global_load_dword v1, v[2:3], off
	v_mbcnt_lo_u32_b32 v2, -1, 0
	v_mov_b32_e32 v3, 0x80
	v_mbcnt_hi_u32_b32 v41, -1, v2
	v_lshl_or_b32 v2, v41, 2, v3
	v_and_b32_e32 v3, 63, v41
	v_cmp_gt_u32_e32 vcc, 48, v3
	s_load_dwordx8 s[72:79], s[0:1], 0x10
	v_and_b32_e32 v42, 63, v0
	v_cndmask_b32_e64 v4, 0, 16, vcc
	v_add_lshl_u32 v4, v4, v41, 2
	v_cmp_gt_u32_e32 vcc, 56, v3
	s_mov_b32 s3, 0
	s_waitcnt vmcnt(1)
	ds_bpermute_b32 v2, v2, v34
	v_cndmask_b32_e64 v5, 0, 8, vcc
	v_add_lshl_u32 v5, v5, v41, 2
	v_cmp_gt_u32_e32 vcc, 60, v3
	s_waitcnt lgkmcnt(0)
	v_add_u32_e32 v2, v2, v34
	ds_bpermute_b32 v4, v4, v2
	s_waitcnt lgkmcnt(0)
	v_add_u32_e32 v2, v4, v2
	ds_bpermute_b32 v4, v5, v2
	v_cndmask_b32_e64 v5, 0, 4, vcc
	v_add_lshl_u32 v5, v5, v41, 2
	v_cmp_gt_u32_e32 vcc, 62, v3
	s_waitcnt lgkmcnt(0)
	v_add_u32_e32 v2, v4, v2
	ds_bpermute_b32 v4, v5, v2
	v_cndmask_b32_e64 v5, 0, 2, vcc
	v_add_lshl_u32 v5, v5, v41, 2
	v_cmp_ne_u32_e32 vcc, 63, v3
	s_waitcnt lgkmcnt(0)
	v_add_u32_e32 v2, v4, v2
	ds_bpermute_b32 v4, v5, v2
	v_addc_co_u32_e32 v3, vcc, 0, v41, vcc
	v_lshlrev_b32_e32 v3, 2, v3
	v_cmp_eq_u32_e32 vcc, 0, v42
	s_waitcnt lgkmcnt(0)
	v_add_u32_e32 v2, v4, v2
	ds_bpermute_b32 v3, v3, v2
	s_waitcnt lgkmcnt(0)
	v_add_u32_e32 v2, v3, v2
	v_cmp_ne_u32_e64 s[4:5], 0, v2
	s_and_b64 s[4:5], vcc, s[4:5]
	s_and_saveexec_b64 s[6:7], s[4:5]
	s_cbranch_execz .LBB1_7
	s_mov_b64 s[4:5], exec

.LBB1_7:
	s_or_b64 exec, exec, s[6:7]
	v_mul_u32_u24_e32 v38, 0x30d4, v0
	v_mov_b32_e32 v39, 0
	v_ashrrev_i32_e32 v35, 31, v34
	s_waitcnt vmcnt(0)
	v_sub_u32_e32 v1, v1, v34
	s_waitcnt lgkmcnt(0)
	v_lshl_add_u64 v[2:3], s[84:85], 0, v[38:39]
	v_lshl_add_u64 v[44:45], v[34:35], 2, v[2:3]
	global_load_dwordx4 v[18:21], v[44:45], off offset:48
	global_load_dwordx4 v[22:25], v[44:45], off offset:32
	global_load_dwordx4 v[26:29], v[44:45], off offset:16
	global_load_dwordx4 v[30:33], v[44:45], off
	global_load_dwordx4 v[2:5], v[44:45], off offset:112
	global_load_dwordx4 v[6:9], v[44:45], off offset:96
	global_load_dwordx4 v[10:13], v[44:45], off offset:80
	global_load_dwordx4 v[14:17], v[44:45], off offset:64
	v_or_b32_e32 v43, 0x4000, v40
	v_mov_b32_e32 v44, 2
	v_mov_b32_e32 v45, 1
	s_mov_b64 s[0:1], exec
	v_cmp_lt_i32_e64 s[30:31], 0, v1
	v_cmp_lt_i32_e64 s[66:67], 1, v1
	v_cmp_lt_i32_e64 s[64:65], 2, v1
	v_cmp_lt_i32_e64 s[62:63], 3, v1
	v_cmp_lt_i32_e64 s[60:61], 4, v1
	v_cmp_lt_i32_e64 s[58:59], 5, v1
	v_cmp_lt_i32_e64 s[56:57], 6, v1
	v_cmp_lt_i32_e64 s[54:55], 7, v1
	v_cmp_lt_i32_e64 s[52:53], 8, v1
	v_cmp_lt_i32_e64 s[50:51], 9, v1
	v_cmp_lt_i32_e64 s[48:49], 10, v1
	v_cmp_lt_i32_e64 s[46:47], 11, v1
	v_cmp_lt_i32_e64 s[44:45], 12, v1
	v_cmp_lt_i32_e64 s[42:43], 13, v1
	v_cmp_lt_i32_e64 s[40:41], 14, v1
	v_cmp_lt_i32_e64 s[38:39], 15, v1
	v_cmp_lt_i32_e64 s[36:37], 16, v1
	v_cmp_lt_i32_e64 s[34:35], 17, v1
	v_cmp_lt_i32_e64 s[28:29], 18, v1
	v_cmp_lt_i32_e64 s[26:27], 19, v1
	v_cmp_lt_i32_e64 s[24:25], 20, v1
	v_cmp_lt_i32_e64 s[22:23], 21, v1
	v_cmp_lt_i32_e64 s[20:21], 22, v1
	v_cmp_lt_i32_e64 s[18:19], 23, v1
	v_cmp_lt_i32_e64 s[16:17], 24, v1
	v_cmp_lt_i32_e64 s[14:15], 25, v1
	v_cmp_lt_i32_e64 s[12:13], 26, v1
	v_cmp_lt_i32_e64 s[10:11], 27, v1
	v_cmp_lt_i32_e64 s[8:9], 28, v1
	v_cmp_lt_i32_e64 s[6:7], 29, v1
	v_cmp_lt_i32_e64 s[4:5], 30, v1
	v_cmp_lt_i32_e64 s[68:69], 31, v1
	s_waitcnt vmcnt(4)
	s_mov_b64 exec, s[30:31]
	v_lshlrev_b32_sdwa v46, v44, v30 dst_sel:DWORD dst_unused:UNUSED_PAD src0_sel:DWORD src1_sel:BYTE_0
	s_nop 0
	ds_add_u32 v46, v45 offset:16384
	s_mov_b64 exec, s[66:67]
	v_lshlrev_b32_sdwa v47, v44, v31 dst_sel:DWORD dst_unused:UNUSED_PAD src0_sel:DWORD src1_sel:BYTE_0
	s_nop 0
	ds_add_u32 v47, v45 offset:16384
	s_mov_b64 exec, s[64:65]
	v_lshlrev_b32_sdwa v46, v44, v32 dst_sel:DWORD dst_unused:UNUSED_PAD src0_sel:DWORD src1_sel:BYTE_0
	s_nop 0
	ds_add_u32 v46, v45 offset:16384
	s_mov_b64 exec, s[62:63]
	v_lshlrev_b32_sdwa v47, v44, v33 dst_sel:DWORD dst_unused:UNUSED_PAD src0_sel:DWORD src1_sel:BYTE_0
	s_nop 0
	ds_add_u32 v47, v45 offset:16384
	s_cmp_eq_u64 s[60:61], 0
	s_cbranch_scc1 .Lcsr_p1_done
	s_mov_b64 exec, s[60:61]
	v_lshlrev_b32_sdwa v46, v44, v26 dst_sel:DWORD dst_unused:UNUSED_PAD src0_sel:DWORD src1_sel:BYTE_0
	s_nop 0
	ds_add_u32 v46, v45 offset:16384
	s_mov_b64 exec, s[58:59]
	v_lshlrev_b32_sdwa v47, v44, v27 dst_sel:DWORD dst_unused:UNUSED_PAD src0_sel:DWORD src1_sel:BYTE_0
	s_nop 0
	ds_add_u32 v47, v45 offset:16384
	s_mov_b64 exec, s[56:57]
	v_lshlrev_b32_sdwa v46, v44, v28 dst_sel:DWORD dst_unused:UNUSED_PAD src0_sel:DWORD src1_sel:BYTE_0
	s_nop 0
	ds_add_u32 v46, v45 offset:16384
	s_mov_b64 exec, s[54:55]
	v_lshlrev_b32_sdwa v47, v44, v29 dst_sel:DWORD dst_unused:UNUSED_PAD src0_sel:DWORD src1_sel:BYTE_0
	s_nop 0
	ds_add_u32 v47, v45 offset:16384
	s_cmp_eq_u64 s[52:53], 0
	s_cbranch_scc1 .Lcsr_p1_done
	s_mov_b64 exec, s[52:53]
	v_lshlrev_b32_sdwa v46, v44, v22 dst_sel:DWORD dst_unused:UNUSED_PAD src0_sel:DWORD src1_sel:BYTE_0
	s_nop 0
	ds_add_u32 v46, v45 offset:16384
	s_mov_b64 exec, s[50:51]
	v_lshlrev_b32_sdwa v47, v44, v23 dst_sel:DWORD dst_unused:UNUSED_PAD src0_sel:DWORD src1_sel:BYTE_0
	s_nop 0
	ds_add_u32 v47, v45 offset:16384
	s_mov_b64 exec, s[48:49]
	v_lshlrev_b32_sdwa v46, v44, v24 dst_sel:DWORD dst_unused:UNUSED_PAD src0_sel:DWORD src1_sel:BYTE_0
	s_nop 0
	ds_add_u32 v46, v45 offset:16384
	s_mov_b64 exec, s[46:47]
	v_lshlrev_b32_sdwa v47, v44, v25 dst_sel:DWORD dst_unused:UNUSED_PAD src0_sel:DWORD src1_sel:BYTE_0
	s_nop 0
	ds_add_u32 v47, v45 offset:16384
	s_cmp_eq_u64 s[44:45], 0
	s_cbranch_scc1 .Lcsr_p1_done
	s_mov_b64 exec, s[44:45]
	v_lshlrev_b32_sdwa v46, v44, v18 dst_sel:DWORD dst_unused:UNUSED_PAD src0_sel:DWORD src1_sel:BYTE_0
	s_nop 0
	ds_add_u32 v46, v45 offset:16384
	s_mov_b64 exec, s[42:43]
	v_lshlrev_b32_sdwa v47, v44, v19 dst_sel:DWORD dst_unused:UNUSED_PAD src0_sel:DWORD src1_sel:BYTE_0
	s_nop 0
	ds_add_u32 v47, v45 offset:16384
	s_mov_b64 exec, s[40:41]
	v_lshlrev_b32_sdwa v46, v44, v20 dst_sel:DWORD dst_unused:UNUSED_PAD src0_sel:DWORD src1_sel:BYTE_0
	s_nop 0
	ds_add_u32 v46, v45 offset:16384
	s_mov_b64 exec, s[38:39]
	v_lshlrev_b32_sdwa v47, v44, v21 dst_sel:DWORD dst_unused:UNUSED_PAD src0_sel:DWORD src1_sel:BYTE_0
	s_nop 0
	ds_add_u32 v47, v45 offset:16384
	s_waitcnt vmcnt(0)
	s_cmp_eq_u64 s[36:37], 0
	s_cbranch_scc1 .Lcsr_p1_done
	s_mov_b64 exec, s[36:37]
	v_lshlrev_b32_sdwa v46, v44, v14 dst_sel:DWORD dst_unused:UNUSED_PAD src0_sel:DWORD src1_sel:BYTE_0
	s_nop 0
	ds_add_u32 v46, v45 offset:16384
	s_mov_b64 exec, s[34:35]
	v_lshlrev_b32_sdwa v47, v44, v15 dst_sel:DWORD dst_unused:UNUSED_PAD src0_sel:DWORD src1_sel:BYTE_0
	s_nop 0
	ds_add_u32 v47, v45 offset:16384
	s_mov_b64 exec, s[28:29]
	v_lshlrev_b32_sdwa v46, v44, v16 dst_sel:DWORD dst_unused:UNUSED_PAD src0_sel:DWORD src1_sel:BYTE_0
	s_nop 0
	ds_add_u32 v46, v45 offset:16384
	s_mov_b64 exec, s[26:27]
	v_lshlrev_b32_sdwa v47, v44, v17 dst_sel:DWORD dst_unused:UNUSED_PAD src0_sel:DWORD src1_sel:BYTE_0
	s_nop 0
	ds_add_u32 v47, v45 offset:16384
	s_cmp_eq_u64 s[24:25], 0
	s_cbranch_scc1 .Lcsr_p1_done
	s_mov_b64 exec, s[24:25]
	v_lshlrev_b32_sdwa v46, v44, v10 dst_sel:DWORD dst_unused:UNUSED_PAD src0_sel:DWORD src1_sel:BYTE_0
	s_nop 0
	ds_add_u32 v46, v45 offset:16384
	s_mov_b64 exec, s[22:23]
	v_lshlrev_b32_sdwa v47, v44, v11 dst_sel:DWORD dst_unused:UNUSED_PAD src0_sel:DWORD src1_sel:BYTE_0
	s_nop 0
	ds_add_u32 v47, v45 offset:16384
	s_mov_b64 exec, s[20:21]
	v_lshlrev_b32_sdwa v46, v44, v12 dst_sel:DWORD dst_unused:UNUSED_PAD src0_sel:DWORD src1_sel:BYTE_0
	s_nop 0
	ds_add_u32 v46, v45 offset:16384
	s_mov_b64 exec, s[18:19]
	v_lshlrev_b32_sdwa v47, v44, v13 dst_sel:DWORD dst_unused:UNUSED_PAD src0_sel:DWORD src1_sel:BYTE_0
	s_nop 0
	ds_add_u32 v47, v45 offset:16384
	s_cmp_eq_u64 s[16:17], 0
	s_cbranch_scc1 .Lcsr_p1_done
	s_mov_b64 exec, s[16:17]
	v_lshlrev_b32_sdwa v46, v44, v6 dst_sel:DWORD dst_unused:UNUSED_PAD src0_sel:DWORD src1_sel:BYTE_0
	s_nop 0
	ds_add_u32 v46, v45 offset:16384
	s_mov_b64 exec, s[14:15]
	v_lshlrev_b32_sdwa v47, v44, v7 dst_sel:DWORD dst_unused:UNUSED_PAD src0_sel:DWORD src1_sel:BYTE_0
	s_nop 0
	ds_add_u32 v47, v45 offset:16384
	s_mov_b64 exec, s[12:13]
	v_lshlrev_b32_sdwa v46, v44, v8 dst_sel:DWORD dst_unused:UNUSED_PAD src0_sel:DWORD src1_sel:BYTE_0
	s_nop 0
	ds_add_u32 v46, v45 offset:16384
	s_mov_b64 exec, s[10:11]
	v_lshlrev_b32_sdwa v47, v44, v9 dst_sel:DWORD dst_unused:UNUSED_PAD src0_sel:DWORD src1_sel:BYTE_0
	s_nop 0
	ds_add_u32 v47, v45 offset:16384
	s_cmp_eq_u64 s[8:9], 0
	s_cbranch_scc1 .Lcsr_p1_done
	s_mov_b64 exec, s[8:9]
	v_lshlrev_b32_sdwa v46, v44, v2 dst_sel:DWORD dst_unused:UNUSED_PAD src0_sel:DWORD src1_sel:BYTE_0
	s_nop 0
	ds_add_u32 v46, v45 offset:16384
	s_mov_b64 exec, s[6:7]
	v_lshlrev_b32_sdwa v47, v44, v3 dst_sel:DWORD dst_unused:UNUSED_PAD src0_sel:DWORD src1_sel:BYTE_0
	s_nop 0
	ds_add_u32 v47, v45 offset:16384
	s_mov_b64 exec, s[4:5]
	v_lshlrev_b32_sdwa v46, v44, v4 dst_sel:DWORD dst_unused:UNUSED_PAD src0_sel:DWORD src1_sel:BYTE_0
	s_nop 0
	ds_add_u32 v46, v45 offset:16384
	s_mov_b64 exec, s[68:69]
	v_lshlrev_b32_sdwa v47, v44, v5 dst_sel:DWORD dst_unused:UNUSED_PAD src0_sel:DWORD src1_sel:BYTE_0
	s_nop 0
	ds_add_u32 v47, v45 offset:16384

_Z5k_outPKfPK15HIP_vector_typeIiLj2EEPKtS0_S0_Pf:
	v_lshl_or_b32 v6, s2, 8, v0
	v_ashrrev_i32_e32 v2, 3, v6
	s_mov_b32 s2, 0xc350
	v_cmp_gt_i32_e32 vcc, s2, v2
	s_and_saveexec_b64 s[2:3], vcc
	s_cbranch_execz .LBB4_7
	s_load_dwordx4 s[4:7], s[0:1], 0x0
	s_load_dwordx4 s[8:11], s[0:1], 0x18
	s_load_dwordx2 s[12:13], s[0:1], 0x10
	v_and_b32_e32 v0, 7, v0
	v_ashrrev_i32_e32 v3, 31, v2
	v_ashrrev_i32_e32 v7, 31, v6
	v_cmp_ne_u32_e32 vcc, 7, v0
	s_waitcnt lgkmcnt(0)
	v_lshl_add_u64 v[4:5], v[2:3], 3, s[6:7]
	v_lshl_add_u64 v[6:7], v[6:7], 2, s[4:5]
	v_cndmask_b32_e32 v1, 0, v0, vcc
	global_load_dwordx2 v[4:5], v[4:5], off
	v_lshlrev_b32_e32 v1, 2, v1
	global_load_dword v8, v[6:7], off
	v_lshl_add_u64 v[6:7], v[2:3], 2, s[8:9]
	global_load_dword v9, v[6:7], off
	global_load_dword v3, v1, s[10:11]
	s_load_dwordx2 s[6:7], s[0:1], 0x28
	s_waitcnt vmcnt(3)
	v_cmp_lt_i32_e64 s[2:3], v4, v5
	s_and_saveexec_b64 s[8:9], s[2:3]
	s_cbranch_execz .LBB4_5
	v_ashrrev_i32_e32 v7, 31, v4
	v_mov_b32_e32 v6, v4
	v_mov_b32_e32 v1, v0
	s_mov_b64 s[2:3], 0
	s_waitcnt lgkmcnt(0)
	v_lshl_add_u64 v[6:7], v[6:7], 1, s[12:13]
	v_mov_b32_e32 v10, 3

amdhsa.kernels:
  - .agpr_count:     0
    .args:
      - .actual_access:  read_only
        .address_space:  global
        .offset:         0
        .size:           8
        .value_kind:     global_buffer
      - .actual_access:  write_only
        .address_space:  global
        .offset:         8
        .size:           8
        .value_kind:     global_buffer
      - .actual_access:  write_only
        .address_space:  global
        .offset:         16
        .size:           8
        .value_kind:     global_buffer
      - .actual_access:  read_only
        .address_space:  global
        .offset:         24
        .size:           8
        .value_kind:     global_buffer
      - .actual_access:  write_only
        .address_space:  global
        .offset:         32
        .size:           8
        .value_kind:     global_buffer
      - .actual_access:  write_only
        .address_space:  global
        .offset:         40
        .size:           8
        .value_kind:     global_buffer
    .group_segment_fixed_size: 14576
    .kernarg_segment_align: 8
    .kernarg_segment_size: 48
    .language:       OpenCL C
    .language_version:
      - 2
      - 0
    .max_flat_workgroup_size: 256
    .name:           _Z5k_binPKiPiPjPKfPDv8_DF16_PDF16_
    .private_segment_fixed_size: 0
    .sgpr_count:     22
    .sgpr_spill_count: 0
    .symbol:         _Z5k_binPKiPiPjPKfPDv8_DF16_PDF16_.kd
    .uniform_work_group_size: 1
    .uses_dynamic_stack: false
    .vgpr_count:     75
    .vgpr_spill_count: 0
    .wavefront_size: 64
  - .agpr_count:     0
    .args:
      - .actual_access:  read_only
        .address_space:  global
        .offset:         0
        .size:           8
        .value_kind:     global_buffer
      - .actual_access:  read_only
        .address_space:  global
        .offset:         8
        .size:           8
        .value_kind:     global_buffer
      - .actual_access:  write_only
        .address_space:  global
        .offset:         16
        .size:           8
        .value_kind:     global_buffer
      - .actual_access:  write_only
        .address_space:  global
        .offset:         24
        .size:           8
        .value_kind:     global_buffer
      - .actual_access:  write_only
        .address_space:  global
        .offset:         32
        .size:           8
        .value_kind:     global_buffer
      - .actual_access:  write_only
        .address_space:  global
        .offset:         40
        .size:           8
        .value_kind:     global_buffer
    .group_segment_fixed_size: 18452
    .kernarg_segment_align: 8
    .kernarg_segment_size: 48
    .language:       OpenCL C
    .language_version:
      - 2
      - 0
    .max_flat_workgroup_size: 256
    .name:           _Z5k_csrPKiPKjP15HIP_vector_typeIiLj2EEPfPtS6_
    .private_segment_fixed_size: 0
    .sgpr_count:     94
    .sgpr_spill_count: 0
    .symbol:         _Z5k_csrPKiPKjP15HIP_vector_typeIiLj2EEPfPtS6_.kd
    .uniform_work_group_size: 1
    .uses_dynamic_stack: false
    .vgpr_count:     65
    .vgpr_spill_count: 0
    .wavefront_size: 64
  - .agpr_count:     0
    .args:
      - .actual_access:  read_only
        .address_space:  global
        .offset:         0
        .size:           8
        .value_kind:     global_buffer
      - .actual_access:  read_only
        .address_space:  global
        .offset:         8
        .size:           8
        .value_kind:     global_buffer
      - .actual_access:  read_only
        .address_space:  global
        .offset:         16
        .size:           8
        .value_kind:     global_buffer
      - .actual_access:  read_only
        .address_space:  global
        .offset:         24
        .size:           8
        .value_kind:     global_buffer
      - .actual_access:  write_only
        .address_space:  global
        .offset:         32
        .size:           8
        .value_kind:     global_buffer
    .group_segment_fixed_size: 129152
    .kernarg_segment_align: 8
    .kernarg_segment_size: 40
    .language:       OpenCL C
    .language_version:
      - 2
      - 0
    .max_flat_workgroup_size: 512
    .name:           _Z6k_gemmPKfPKDv8_DF16_S0_S0_PDF16_
    .private_segment_fixed_size: 0
    .sgpr_count:     22
    .sgpr_spill_count: 0
    .symbol:         _Z6k_gemmPKfPKDv8_DF16_S0_S0_PDF16_.kd
    .uniform_work_group_size: 1
    .uses_dynamic_stack: false
    .vgpr_count:     256
    .vgpr_spill_count: 0
    .wavefront_size: 64
  - .agpr_count:     0
    .args:
      - .actual_access:  read_only
        .address_space:  global
        .offset:         0
        .size:           8
        .value_kind:     global_buffer
      - .actual_access:  read_only
        .address_space:  global
        .offset:         8
        .size:           8
        .value_kind:     global_buffer
      - .actual_access:  read_only
        .address_space:  global
        .offset:         16
        .size:           8
        .value_kind:     global_buffer
      - .actual_access:  read_only
        .address_space:  global
        .offset:         24
        .size:           8
        .value_kind:     global_buffer
      - .actual_access:  read_only
        .address_space:  global
        .offset:         32
        .size:           8
        .value_kind:     global_buffer
      - .actual_access:  read_only
        .address_space:  global
        .offset:         40
        .size:           8
        .value_kind:     global_buffer
      - .address_space:  global
        .offset:         48
        .size:           8
        .value_kind:     global_buffer
    .group_segment_fixed_size: 2304
    .kernarg_segment_align: 8
    .kernarg_segment_size: 56
    .language:       OpenCL C
    .language_version:
      - 2
      - 0
    .max_flat_workgroup_size: 320
    .name:           _Z6k_agg1PKDF16_PK15HIP_vector_typeIiLj2EEPKtPKfS8_S8_Pf
    .private_segment_fixed_size: 0
    .sgpr_count:     41
    .sgpr_spill_count: 0
    .symbol:         _Z6k_agg1PKDF16_PK15HIP_vector_typeIiLj2EEPKtPKfS8_S8_Pf.kd
    .uniform_work_group_size: 1
    .uses_dynamic_stack: false
    .vgpr_count:     63
    .vgpr_spill_count: 0
    .wavefront_size: 64
  - .agpr_count:     0
    .args:
      - .actual_access:  read_only
        .address_space:  global
        .offset:         0
        .size:           8
        .value_kind:     global_buffer
      - .actual_access:  read_only
        .address_space:  global
        .offset:         8
        .size:           8
        .value_kind:     global_buffer
      - .actual_access:  read_only
        .address_space:  global
        .offset:         16
        .size:           8
        .value_kind:     global_buffer
      - .actual_access:  read_only
        .address_space:  global
        .offset:         24
        .size:           8
        .value_kind:     global_buffer
      - .actual_access:  read_only
        .address_space:  global
        .offset:         32
        .size:           8
        .value_kind:     global_buffer
      - .actual_access:  write_only
        .address_space:  global
        .offset:         40
        .size:           8
        .value_kind:     global_buffer
    .group_segment_fixed_size: 0
    .kernarg_segment_align: 8
    .kernarg_segment_size: 48
    .language:       OpenCL C
    .language_version:
      - 2
      - 0
    .max_flat_workgroup_size: 256
    .name:           _Z5k_outPKfPK15HIP_vector_typeIiLj2EEPKtS0_S0_Pf
    .private_segment_fixed_size: 0
    .sgpr_count:     20
    .sgpr_spill_count: 0
    .symbol:         _Z5k_outPKfPK15HIP_vector_typeIiLj2EEPKtS0_S0_Pf.kd
    .uniform_work_group_size: 1
    .uses_dynamic_stack: false
    .vgpr_count:     27
    .vgpr_spill_count: 0
    .wavefront_size: 64
